# MoE K-loop: first iteration peeled with C=0 MFMAs, accumulator clears between units removed; scheduler without LDS round trips
# speedup vs baseline: 1.0064x; 1.0064x over previous
.LBB0_1889:
	s_mov_b32 s6, s28
	s_mov_b32 s55, s88
	s_mov_b32 s10, s34
	s_mov_b32 s7, s29
	s_mov_b32 s8, s30
	s_mov_b64 s[18:19], s[40:41]
	s_mov_b64 s[16:17], s[38:39]
	s_mov_b32 s86, s87

.Lpk_1931:
	s_add_u32 s3, s50, 0x100
	s_addc_u32 s31, s51, 0
	s_and_b64 s[0:1], s[52:53], exec
	s_cselect_b32 s51, s90, s31
	s_cselect_b32 s50, s91, s3
	s_add_u32 s0, s18, s2
	s_addc_u32 s1, s19, 0
	s_add_u32 s2, s0, 0x100
	s_waitcnt vmcnt(8)
	s_addc_u32 s3, s1, 0
	s_waitcnt lgkmcnt(0)
	s_and_b64 s[0:1], s[52:53], exec
	s_cselect_b32 s0, s92, s2
	s_cselect_b32 s1, s35, s3
	s_barrier
	s_setprio 1
	s_waitcnt lgkmcnt(0)
	s_nop 1
	v_mfma_f32_16x16x128_f8f6f4 v[196:199], v[36:43], v[68:75], 0
	s_nop 1
	v_mfma_f32_16x16x128_f8f6f4 v[192:195], v[28:35], v[68:75], 0
	s_nop 1
	v_mfma_f32_16x16x128_f8f6f4 v[188:191], v[36:43], v[60:67], 0
	s_nop 1
	v_mfma_f32_16x16x128_f8f6f4 v[184:187], v[28:35], v[60:67], 0
	s_nop 1
	v_mfma_f32_16x16x128_f8f6f4 v[180:183], v[36:43], v[52:59], 0
	s_nop 1
	v_mfma_f32_16x16x128_f8f6f4 v[176:179], v[28:35], v[52:59], 0
	s_nop 1
	v_mfma_f32_16x16x128_f8f6f4 v[172:175], v[36:43], v[44:51], 0
	s_nop 1
	v_mfma_f32_16x16x128_f8f6f4 v[168:171], v[28:35], v[44:51], 0
	s_setprio 0
	s_setprio 1
	s_nop 1
	v_mfma_f32_16x16x128_f8f6f4 v[164:167], v[20:27], v[68:75], 0
	s_nop 1
	v_mfma_f32_16x16x128_f8f6f4 v[160:163], v[4:11], v[68:75], 0
	s_nop 1
	v_mfma_f32_16x16x128_f8f6f4 v[156:159], v[20:27], v[60:67], 0
	s_nop 1
	v_mfma_f32_16x16x128_f8f6f4 v[152:155], v[4:11], v[60:67], 0
	s_nop 1
	v_mfma_f32_16x16x128_f8f6f4 v[148:151], v[20:27], v[52:59], 0
	s_nop 1
	v_mfma_f32_16x16x128_f8f6f4 v[144:147], v[4:11], v[52:59], 0
	s_nop 1
	v_mfma_f32_16x16x128_f8f6f4 v[140:143], v[20:27], v[44:51], 0
	s_nop 1
	v_mfma_f32_16x16x128_f8f6f4 v[136:139], v[4:11], v[44:51], 0
	s_setprio 0
	s_barrier
	s_mov_b32 m0, s64
	v_lshl_add_u64 v[46:47], s[0:1], 0, v[16:17]
	s_add_u32 s2, s0, 0x20000
	ds_read_b128 v[52:55], v244 offset:16384
	ds_read_b128 v[56:59], v244 offset:17408
	ds_read_b128 v[60:63], v244 offset:18432
	ds_read_b128 v[64:67], v244 offset:19456
	ds_read_b128 v[68:71], v244 offset:20480
	ds_read_b128 v[72:75], v244 offset:21504
	ds_read_b128 v[228:231], v244 offset:22528
	ds_read_b128 v[232:235], v244 offset:23552
	global_load_lds_dwordx4 v[46:47], off
	v_lshl_add_u64 v[44:45], s[0:1], 0, v[208:209]
	s_mov_b32 m0, s65
	s_addc_u32 s3, s1, 0
	global_load_lds_dwordx4 v[44:45], off
	v_lshl_add_u64 v[48:49], s[2:3], 0, v[16:17]
	s_mov_b32 m0, s66
	v_mov_b32_e32 v207, v3
	global_load_lds_dwordx4 v[48:49], off
	v_lshl_add_u64 v[48:49], s[2:3], 0, v[208:209]
	s_mov_b32 m0, s67
	v_mov_b32_e32 v205, v3
	global_load_lds_dwordx4 v[48:49], off
	s_mov_b32 m0, s63
	v_lshl_add_u64 v[50:51], s[50:51], 0, v[206:207]
	global_load_lds_dwordx4 v206, s[50:51]
	s_mov_b32 m0, s70
	v_lshl_add_u64 v[48:49], s[50:51], 0, v[204:205]
	global_load_lds_dwordx4 v204, s[50:51]
	s_waitcnt vmcnt(8)
	s_waitcnt lgkmcnt(0)
	s_barrier
	s_setprio 1
	s_waitcnt lgkmcnt(0)
	s_nop 1
	v_mfma_f32_16x16x128_f8f6f4 v[132:135], v[36:43], v[52:59], 0
	s_nop 1
	v_mfma_f32_16x16x128_f8f6f4 v[128:131], v[28:35], v[52:59], 0
	s_nop 1
	v_mfma_f32_16x16x128_f8f6f4 v[124:127], v[36:43], v[60:67], 0
	s_nop 1
	v_mfma_f32_16x16x128_f8f6f4 v[120:123], v[28:35], v[60:67], 0
	s_nop 1
	v_mfma_f32_16x16x128_f8f6f4 v[116:119], v[36:43], v[68:75], 0
	s_nop 1
	v_mfma_f32_16x16x128_f8f6f4 v[112:115], v[28:35], v[68:75], 0
	s_nop 1
	v_mfma_f32_16x16x128_f8f6f4 v[108:111], v[36:43], v[228:235], 0
	s_nop 1
	v_mfma_f32_16x16x128_f8f6f4 v[104:107], v[28:35], v[228:235], 0
	s_setprio 0
	s_setprio 1
	s_nop 1
	v_mfma_f32_16x16x128_f8f6f4 v[100:103], v[20:27], v[52:59], 0
	s_nop 1
	v_mfma_f32_16x16x128_f8f6f4 v[96:99], v[4:11], v[52:59], 0
	s_nop 1
	v_mfma_f32_16x16x128_f8f6f4 v[92:95], v[20:27], v[60:67], 0
	s_nop 1
	v_mfma_f32_16x16x128_f8f6f4 v[88:91], v[4:11], v[60:67], 0
	s_nop 1
	v_mfma_f32_16x16x128_f8f6f4 v[84:87], v[20:27], v[68:75], 0
	s_nop 1
	v_mfma_f32_16x16x128_f8f6f4 v[80:83], v[4:11], v[68:75], 0
	s_nop 1
	v_mfma_f32_16x16x128_f8f6f4 v[76:79], v[20:27], v[228:235], 0
	s_nop 1
	v_mfma_f32_16x16x128_f8f6f4 v[12:15], v[4:11], v[228:235], 0
	s_setprio 0
	s_barrier
	s_add_i32 s2, 0, 0x18000
	s_add_i32 s3, 0, 0x1c000
	v_add_u32_e32 v24, s2, v239
	v_add_u32_e32 v40, s3, v239
	ds_read_b128 v[4:7], v24
	ds_read_b128 v[8:11], v24 offset:1024
	ds_read_b128 v[20:23], v24 offset:2048
	ds_read_b128 v[24:27], v24 offset:3072
	ds_read_b128 v[28:31], v40
	ds_read_b128 v[32:35], v40 offset:1024
	ds_read_b128 v[36:39], v40 offset:2048
	ds_read_b128 v[40:43], v40 offset:3072
	s_mov_b32 m0, s71
	v_lshl_add_u64 v[200:201], s[50:51], 0, v[2:3]
	ds_read_b128 v[52:55], v244 offset:32768
	ds_read_b128 v[56:59], v244 offset:33792
	ds_read_b128 v[60:63], v244 offset:34816
	ds_read_b128 v[64:67], v244 offset:35840
	ds_read_b128 v[68:71], v244 offset:36864
	ds_read_b128 v[72:75], v244 offset:37888
	ds_read_b128 v[228:231], v244 offset:38912
	ds_read_b128 v[232:235], v244 offset:39936
	global_load_lds_dwordx4 v[200:201], off
	v_lshl_add_u64 v[200:201], s[50:51], 0, v[210:211]
	s_mov_b32 m0, s74
	s_nop 0
	global_load_lds_dwordx4 v[200:201], off
	s_waitcnt vmcnt(8)
	s_waitcnt lgkmcnt(0)
	s_barrier
	s_setprio 1
	s_waitcnt lgkmcnt(0)
	s_nop 1
	v_mfma_f32_16x16x128_f8f6f4 v[196:199], v[4:11], v[52:59], v[196:199]
	s_nop 1
	v_mfma_f32_16x16x128_f8f6f4 v[192:195], v[20:27], v[52:59], v[192:195]
	s_nop 1
	v_mfma_f32_16x16x128_f8f6f4 v[188:191], v[4:11], v[60:67], v[188:191]
	s_nop 1
	v_mfma_f32_16x16x128_f8f6f4 v[184:187], v[20:27], v[60:67], v[184:187]
	s_nop 1
	v_mfma_f32_16x16x128_f8f6f4 v[180:183], v[4:11], v[68:75], v[180:183]
	s_nop 1
	v_mfma_f32_16x16x128_f8f6f4 v[176:179], v[20:27], v[68:75], v[176:179]
	s_nop 1
	v_mfma_f32_16x16x128_f8f6f4 v[172:175], v[4:11], v[228:235], v[172:175]
	s_nop 1
	v_mfma_f32_16x16x128_f8f6f4 v[168:171], v[20:27], v[228:235], v[168:171]
	s_setprio 0
	s_setprio 1
	s_nop 1
	v_mfma_f32_16x16x128_f8f6f4 v[164:167], v[28:35], v[52:59], v[164:167]
	s_nop 1
	v_mfma_f32_16x16x128_f8f6f4 v[160:163], v[36:43], v[52:59], v[160:163]
	s_nop 1
	v_mfma_f32_16x16x128_f8f6f4 v[156:159], v[28:35], v[60:67], v[156:159]
	s_nop 1
	v_mfma_f32_16x16x128_f8f6f4 v[152:155], v[36:43], v[60:67], v[152:155]
	s_nop 1
	v_mfma_f32_16x16x128_f8f6f4 v[148:151], v[28:35], v[68:75], v[148:151]
	s_nop 1
	v_mfma_f32_16x16x128_f8f6f4 v[144:147], v[36:43], v[68:75], v[144:147]
	s_nop 1
	v_mfma_f32_16x16x128_f8f6f4 v[140:143], v[28:35], v[228:235], v[140:143]
	s_nop 1
	v_mfma_f32_16x16x128_f8f6f4 v[136:139], v[36:43], v[228:235], v[136:139]
	s_setprio 0
	s_barrier
	s_mov_b64 s[50:51], 0x80
	s_add_i32 s2, s2, s11
	v_lshl_add_u64 v[46:47], v[46:47], 0, s[50:51]
	s_mov_b32 m0, s2
	ds_read_b128 v[52:55], v244 offset:49152
	ds_read_b128 v[56:59], v244 offset:50176
	ds_read_b128 v[60:63], v244 offset:51200
	ds_read_b128 v[64:67], v244 offset:52224
	ds_read_b128 v[68:71], v244 offset:53248
	ds_read_b128 v[72:75], v244 offset:54272
	ds_read_b128 v[228:231], v244 offset:55296
	ds_read_b128 v[232:235], v244 offset:56320
	global_load_lds_dwordx4 v[46:47], off
	s_add_i32 m0, s2, 0x2000
	s_add_u32 s0, s0, 0x20080
	v_lshl_add_u64 v[44:45], v[44:45], 0, s[50:51]
	s_addc_u32 s1, s1, 0
	s_add_i32 s2, s3, s11
	global_load_lds_dwordx4 v[44:45], off
	v_lshl_add_u64 v[44:45], s[0:1], 0, v[16:17]
	s_mov_b32 m0, s2
	s_nop 0
	global_load_lds_dwordx4 v[44:45], off
	v_lshl_add_u64 v[44:45], s[0:1], 0, v[208:209]
	s_add_i32 m0, s2, 0x2000
	s_nop 0
	global_load_lds_dwordx4 v[44:45], off
	v_lshl_add_u64 v[44:45], v[50:51], 0, s[50:51]
	s_mov_b32 m0, s82
	s_nop 0
	global_load_lds_dwordx4 v[44:45], off
	v_lshl_add_u64 v[44:45], v[48:49], 0, s[50:51]
	s_mov_b32 m0, s83
	s_nop 0
	global_load_lds_dwordx4 v[44:45], off
	s_waitcnt vmcnt(8)
	s_waitcnt lgkmcnt(0)
	s_barrier
	s_setprio 1
	s_waitcnt lgkmcnt(0)
	s_nop 1
	v_mfma_f32_16x16x128_f8f6f4 v[132:135], v[4:11], v[52:59], v[132:135]
	s_nop 1
	v_mfma_f32_16x16x128_f8f6f4 v[128:131], v[20:27], v[52:59], v[128:131]
	s_nop 1
	v_mfma_f32_16x16x128_f8f6f4 v[124:127], v[4:11], v[60:67], v[124:127]
	s_nop 1
	v_mfma_f32_16x16x128_f8f6f4 v[120:123], v[20:27], v[60:67], v[120:123]
	s_nop 1
	v_mfma_f32_16x16x128_f8f6f4 v[116:119], v[4:11], v[68:75], v[116:119]
	s_nop 1
	v_mfma_f32_16x16x128_f8f6f4 v[112:115], v[20:27], v[68:75], v[112:115]
	s_nop 1
	v_mfma_f32_16x16x128_f8f6f4 v[108:111], v[4:11], v[228:235], v[108:111]
	s_nop 1
	v_mfma_f32_16x16x128_f8f6f4 v[104:107], v[20:27], v[228:235], v[104:107]
	s_setprio 0
	s_setprio 1
	s_nop 1
	v_mfma_f32_16x16x128_f8f6f4 v[100:103], v[28:35], v[52:59], v[100:103]
	s_nop 1
	v_mfma_f32_16x16x128_f8f6f4 v[96:99], v[36:43], v[52:59], v[96:99]
	s_nop 1
	v_mfma_f32_16x16x128_f8f6f4 v[92:95], v[28:35], v[60:67], v[92:95]
	s_nop 1
	v_mfma_f32_16x16x128_f8f6f4 v[88:91], v[36:43], v[60:67], v[88:91]
	s_nop 1
	v_mfma_f32_16x16x128_f8f6f4 v[84:87], v[28:35], v[68:75], v[84:87]
	s_nop 1
	v_mfma_f32_16x16x128_f8f6f4 v[80:83], v[36:43], v[68:75], v[80:83]
	s_nop 1
	v_mfma_f32_16x16x128_f8f6f4 v[76:79], v[28:35], v[228:235], v[76:79]
	s_nop 1
	v_mfma_f32_16x16x128_f8f6f4 v[12:15], v[36:43], v[228:235], v[12:15]
	s_setprio 0
	s_barrier
	s_add_i32 s0, s89, 2
	s_cmp_gt_u32 s89, 5
	s_cbranch_scc1 .LBB0_1937
	s_mov_b32 s89, s0
	s_branch .LBB0_1899

.Lpk_1936:
	ds_read_b32 v200, v243
	s_waitcnt lgkmcnt(0)
	v_and_b32_e32 v207, 0x3fff, v200
	s_branch .Lpk_1930
.LBB0_1899:
	s_cmp_eq_u32 s89, 4
	s_cselect_b64 s[0:1], -1, 0
	s_and_b64 s[0:1], s[42:43], s[0:1]
	s_and_b64 s[2:3], s[0:1], s[44:45]
	s_and_b64 s[2:3], s[2:3], s[12:13]
	s_andn2_b64 vcc, exec, s[2:3]
	s_cbranch_vccnz .LBB0_1901
	s_mov_b32 m0, s84
	s_nop 0
	global_load_lds_dword v[214:215], off
